# GEMM2 (down-proj) walks the expert row panels in reverse order, so the panels GEMM1 wrote last (still cached beyond L2) are read first (on top of v34)
# baseline (speedup 1.0000x reference)
.LBB0_2066:
	s_andn2_b64 vcc, exec, s[6:7]
	v_readlane_b32 s6, v252, 61
	s_mov_b32 s40, s6
	v_readlane_b32 s6, v253, 21
	s_mov_b32 s36, s6
	s_cbranch_vccnz .LBB0_2068
	v_readlane_b32 s6, v252, 62
	s_cmp_lt_i32 s6, s9
	s_cselect_b64 s[4:5], -1, 0
	s_sub_i32 s40, s9, s6
	s_add_i32 s40, s40, -1
	v_readlane_b32 s6, v252, 63
	s_mov_b32 s36, s6

.LBB0_2080:
	s_lshl_b32 s0, s23, 6
	v_readlane_b32 s1, v252, 62
	s_add_i32 s12, s1, s0
	s_cmp_lt_i32 s12, s13
	s_cselect_b64 s[0:1], -1, 0
	s_sub_i32 s12, s13, s12
	s_add_i32 s12, s12, -1
	v_readlane_b32 s13, v252, 63
	s_mov_b32 s28, s13
	s_andn2_b64 vcc, exec, s[0:1]
	s_mov_b64 s[48:49], 0
	s_cbranch_vccz .LBB0_2083
	s_branch .LBB0_2084
